# speedup vs baseline: 1.0175x; 1.0175x over previous
_Z5k_mlpPKfPKtPKiS4_S4_S4_S2_S2_S2_S0_S0_S0_S0_S0_S0_S0_S4_S4_Pf:
	s_load_dwordx8 s[4:11], s[0:1], 0x48
	s_load_dwordx4 s[12:15], s[0:1], 0x68
	s_load_dwordx2 s[18:19], s[0:1], 0x80
	v_lshlrev_b32_e32 v6, 2, v0
	s_and_b32 s3, s2, 0xff
	s_mul_i32 s3, s3, 6
	v_mov_b64_e32 v[66:67], 0
	s_ashr_i32 s16, s2, 8
	s_add_i32 s3, s3, s16
	s_cmpk_lt_i32 s2, 0x600
	s_cselect_b32 s2, s3, s2
	v_lshrrev_b32_e32 v1, 6, v0
	v_lshl_or_b32 v3, s2, 1, v1
	v_lshlrev_b32_e32 v2, 5, v3
	v_mov_b32_e32 v7, 32
	s_waitcnt lgkmcnt(0)
	s_load_dword s22, s[18:19], 0x0
	s_load_dword s24, s[18:19], 0x4
	s_load_dword s26, s[18:19], 0x8
	s_load_dword s28, s[18:19], 0xc
	s_load_dword s30, s[18:19], 0x10
	s_load_dword s34, s[18:19], 0x14
	s_load_dword s36, s[18:19], 0x18
	s_load_dword s38, s[18:19], 0x1c
	s_load_dword s33, s[18:19], 0x20
	global_load_dword v8, v6, s[4:5]
	global_load_dword v9, v6, s[6:7]
	global_load_dword v10, v6, s[8:9]
	global_load_dword v11, v6, s[10:11]
	global_load_dword v12, v6, s[12:13]
	global_load_dword v13, v6, s[14:15]
	s_waitcnt lgkmcnt(0)
	s_mov_b64 s[4:5], -1
	s_mul_i32 s2, s22, 39
	s_mul_hi_i32 s2, s2, 0x66666667
	s_lshr_b32 s3, s2, 31
	s_ashr_i32 s23, s2, 9
	s_add_i32 s23, s23, s3
	v_cmp_le_i32_e32 vcc, s23, v3
	s_and_saveexec_b64 s[2:3], vcc
	s_cbranch_execz .LBB2_66
	v_subrev_u32_e32 v3, s23, v3
	v_mov_b32_e32 v7, 32
	v_lshlrev_b32_e32 v2, 5, v3
	v_mov_b64_e32 v[66:67], 1
	s_waitcnt lgkmcnt(0)
	s_mul_i32 s4, s24, 39
	s_mul_hi_i32 s4, s4, 0x66666667
	s_lshr_b32 s5, s4, 31
	s_ashr_i32 s25, s4, 9
	s_add_i32 s25, s25, s5
	v_cmp_le_i32_e32 vcc, s25, v3
	s_mov_b64 s[6:7], -1
	s_and_saveexec_b64 s[4:5], vcc
	s_cbranch_execz .LBB2_65
	v_subrev_u32_e32 v3, s25, v3
	v_mov_b32_e32 v7, 32
	v_lshlrev_b32_e32 v2, 5, v3
	v_mov_b64_e32 v[66:67], 2
	s_waitcnt lgkmcnt(0)
	s_mul_i32 s6, s26, 39
	s_mul_hi_i32 s6, s6, 0x66666667
	s_lshr_b32 s7, s6, 31
	s_ashr_i32 s27, s6, 9
	s_add_i32 s27, s27, s7
	v_cmp_le_i32_e32 vcc, s27, v3
	s_mov_b64 s[8:9], -1
	s_and_saveexec_b64 s[6:7], vcc
	s_cbranch_execz .LBB2_64
	v_subrev_u32_e32 v3, s27, v3
	v_mov_b32_e32 v7, 32
	v_lshlrev_b32_e32 v2, 5, v3
	v_mov_b64_e32 v[66:67], 3
	s_waitcnt lgkmcnt(0)
	s_mul_i32 s8, s28, 39
	s_mul_hi_i32 s8, s8, 0x66666667
	s_lshr_b32 s9, s8, 31
	s_ashr_i32 s29, s8, 9
	s_add_i32 s29, s29, s9
	v_cmp_le_i32_e32 vcc, s29, v3
	s_mov_b64 s[10:11], -1
	s_and_saveexec_b64 s[8:9], vcc
	s_cbranch_execz .LBB2_63
	v_subrev_u32_e32 v3, s29, v3
	v_mov_b32_e32 v7, 32
	v_lshlrev_b32_e32 v2, 5, v3
	v_mov_b64_e32 v[66:67], 4
	s_waitcnt lgkmcnt(0)
	s_mul_i32 s10, s30, 39
	s_mul_hi_i32 s10, s10, 0x66666667
	s_lshr_b32 s11, s10, 31
	s_ashr_i32 s31, s10, 9
	s_add_i32 s31, s31, s11
	v_cmp_le_i32_e32 vcc, s31, v3
	s_mov_b64 s[12:13], -1
	s_and_saveexec_b64 s[10:11], vcc
	s_cbranch_execz .LBB2_62
	v_subrev_u32_e32 v3, s31, v3
	v_mov_b32_e32 v7, 32
	v_lshlrev_b32_e32 v2, 5, v3
	v_mov_b64_e32 v[66:67], 5
	s_waitcnt lgkmcnt(0)
	s_mul_i32 s12, s34, 39
	s_mul_hi_i32 s12, s12, 0x66666667
	s_lshr_b32 s13, s12, 31
	s_ashr_i32 s35, s12, 9
	s_add_i32 s35, s35, s13
	v_cmp_le_i32_e32 vcc, s35, v3
	s_mov_b64 s[14:15], -1
	s_and_saveexec_b64 s[12:13], vcc
	s_cbranch_execz .LBB2_61
	v_subrev_u32_e32 v3, s35, v3
	v_mov_b32_e32 v7, 32
	v_lshlrev_b32_e32 v2, 5, v3
	v_mov_b64_e32 v[66:67], 6
	s_waitcnt lgkmcnt(0)
	s_mul_i32 s14, s36, 39
	s_mul_hi_i32 s14, s14, 0x66666667
	s_lshr_b32 s15, s14, 31
	s_ashr_i32 s37, s14, 9
	s_add_i32 s37, s37, s15
	v_cmp_le_i32_e32 vcc, s37, v3
	s_mov_b64 s[16:17], -1
	s_and_saveexec_b64 s[14:15], vcc
	s_cbranch_execz .LBB2_60
	v_subrev_u32_e32 v3, s37, v3
	v_mov_b32_e32 v7, 32
	v_lshlrev_b32_e32 v2, 5, v3
	v_mov_b64_e32 v[66:67], 7
	s_waitcnt lgkmcnt(0)
	s_mul_i32 s16, s38, 39
	s_mul_hi_i32 s16, s16, 0x66666667
	s_lshr_b32 s17, s16, 31
	s_ashr_i32 s39, s16, 9
	s_add_i32 s39, s39, s17
	v_cmp_le_i32_e32 vcc, s39, v3
	s_mov_b64 s[20:21], -1
	s_and_saveexec_b64 s[16:17], vcc
	s_cbranch_execz .LBB2_59
	v_subrev_u32_e32 v3, s39, v3
	v_mov_b32_e32 v7, 32
	v_lshlrev_b32_e32 v2, 5, v3
	v_mov_b64_e32 v[66:67], 8
	s_waitcnt lgkmcnt(0)
	s_mul_i32 s18, s33, 39
	s_mul_hi_i32 s18, s18, 0x66666667
	s_lshr_b32 s19, s18, 31
	s_ashr_i32 s40, s18, 9
	s_add_i32 s40, s40, s19
	v_cmp_le_i32_e32 vcc, s40, v3
	s_and_saveexec_b64 s[18:19], vcc
	s_cbranch_execz .LBB2_58
	s_lshl_b32 s23, s23, 5
	s_sub_i32 s22, s22, s23
	s_add_i32 s20, s22, 7
	s_ashr_i32 s21, s20, 31
	s_lshr_b32 s21, s21, 29
	s_add_i32 s20, s20, s21
	v_subrev_u32_e32 v3, s40, v3
	s_ashr_i32 s41, s20, 3
	v_cmp_le_i32_e32 vcc, s41, v3
	s_and_saveexec_b64 s[20:21], vcc
	s_xor_b64 s[20:21], exec, s[20:21]
	v_subrev_u32_e32 v3, s41, v3
	s_or_saveexec_b64 s[20:21], s[20:21]
	v_mov_b32_e32 v7, 32
	s_xor_b64 exec, exec, s[20:21]
	v_lshlrev_b32_e32 v4, 3, v3
	v_add_u32_e32 v2, s23, v4
	v_sub_u32_e32 v4, s22, v4
	v_min_i32_e32 v7, 8, v4
	s_or_b64 exec, exec, s[20:21]
	v_mov_b64_e32 v[66:67], 0
	s_mov_b64 s[22:23], -1
	s_and_saveexec_b64 s[20:21], vcc
	s_cbranch_execz .LBB2_57
	s_lshl_b32 s25, s25, 5
	s_sub_i32 s24, s24, s25
	s_add_i32 s22, s24, 7
	s_ashr_i32 s23, s22, 31
	s_lshr_b32 s23, s23, 29
	s_add_i32 s22, s22, s23
	s_ashr_i32 s41, s22, 3
	v_cmp_le_i32_e32 vcc, s41, v3
	s_and_saveexec_b64 s[22:23], vcc
	s_xor_b64 s[22:23], exec, s[22:23]
	v_subrev_u32_e32 v3, s41, v3
	s_andn2_saveexec_b64 s[22:23], s[22:23]
	v_lshlrev_b32_e32 v4, 3, v3
	v_add_u32_e32 v2, s25, v4
	v_sub_u32_e32 v4, s24, v4
	v_min_i32_e32 v7, 8, v4
	s_or_b64 exec, exec, s[22:23]
	v_mov_b64_e32 v[66:67], 1
	s_mov_b64 s[24:25], -1
	s_and_saveexec_b64 s[22:23], vcc
	s_cbranch_execz .LBB2_56
	s_lshl_b32 s27, s27, 5
	s_sub_i32 s26, s26, s27
	s_add_i32 s24, s26, 7
	s_ashr_i32 s25, s24, 31
	s_lshr_b32 s25, s25, 29
	s_add_i32 s24, s24, s25
	s_ashr_i32 s41, s24, 3
	v_cmp_le_i32_e32 vcc, s41, v3
	s_and_saveexec_b64 s[24:25], vcc
	s_xor_b64 s[24:25], exec, s[24:25]
	v_subrev_u32_e32 v3, s41, v3
	s_andn2_saveexec_b64 s[24:25], s[24:25]
	v_lshlrev_b32_e32 v4, 3, v3
	v_add_u32_e32 v2, s27, v4
	v_sub_u32_e32 v4, s26, v4
	v_min_i32_e32 v7, 8, v4
	s_or_b64 exec, exec, s[24:25]
	v_mov_b64_e32 v[66:67], 2
	s_mov_b64 s[26:27], -1
	s_and_saveexec_b64 s[24:25], vcc
	s_cbranch_execz .LBB2_55
	s_lshl_b32 s29, s29, 5
	s_sub_i32 s28, s28, s29
	s_add_i32 s26, s28, 7
	s_ashr_i32 s27, s26, 31
	s_lshr_b32 s27, s27, 29
	s_add_i32 s26, s26, s27
	s_ashr_i32 s41, s26, 3
	v_cmp_le_i32_e32 vcc, s41, v3
	s_and_saveexec_b64 s[26:27], vcc
	s_xor_b64 s[26:27], exec, s[26:27]
	v_subrev_u32_e32 v3, s41, v3
	s_andn2_saveexec_b64 s[26:27], s[26:27]
	v_lshlrev_b32_e32 v4, 3, v3
	v_add_u32_e32 v2, s29, v4
	v_sub_u32_e32 v4, s28, v4
	v_min_i32_e32 v7, 8, v4
	s_or_b64 exec, exec, s[26:27]
	v_mov_b64_e32 v[66:67], 3
	s_mov_b64 s[28:29], -1
	s_and_saveexec_b64 s[26:27], vcc
	s_cbranch_execz .LBB2_54
	s_lshl_b32 s31, s31, 5
	s_sub_i32 s30, s30, s31
	s_add_i32 s28, s30, 7
	s_ashr_i32 s29, s28, 31
	s_lshr_b32 s29, s29, 29
	s_add_i32 s28, s28, s29
	s_ashr_i32 s41, s28, 3
	v_cmp_le_i32_e32 vcc, s41, v3
	s_and_saveexec_b64 s[28:29], vcc
	s_xor_b64 s[28:29], exec, s[28:29]
	v_subrev_u32_e32 v3, s41, v3
	s_andn2_saveexec_b64 s[28:29], s[28:29]
	v_lshlrev_b32_e32 v4, 3, v3
	v_add_u32_e32 v2, s31, v4
	v_sub_u32_e32 v4, s30, v4
	v_min_i32_e32 v7, 8, v4
	s_or_b64 exec, exec, s[28:29]
	v_mov_b64_e32 v[66:67], 4
	s_mov_b64 s[30:31], -1
	s_and_saveexec_b64 s[28:29], vcc
	s_cbranch_execz .LBB2_53
	s_lshl_b32 s35, s35, 5
	s_sub_i32 s34, s34, s35
	s_add_i32 s30, s34, 7
	s_ashr_i32 s31, s30, 31
	s_lshr_b32 s31, s31, 29
	s_add_i32 s30, s30, s31
	s_ashr_i32 s41, s30, 3
	v_cmp_le_i32_e32 vcc, s41, v3
	s_and_saveexec_b64 s[30:31], vcc
	s_xor_b64 s[30:31], exec, s[30:31]
	v_subrev_u32_e32 v3, s41, v3
	s_andn2_saveexec_b64 s[30:31], s[30:31]
	v_lshlrev_b32_e32 v4, 3, v3
	v_add_u32_e32 v2, s35, v4
	v_sub_u32_e32 v4, s34, v4
	v_min_i32_e32 v7, 8, v4
	s_or_b64 exec, exec, s[30:31]
	v_mov_b64_e32 v[66:67], 5
	s_mov_b64 s[34:35], -1
	s_and_saveexec_b64 s[30:31], vcc
	s_cbranch_execz .LBB2_52
	s_lshl_b32 s37, s37, 5
	s_sub_i32 s36, s36, s37
	s_add_i32 s34, s36, 7
	s_ashr_i32 s35, s34, 31
	s_lshr_b32 s35, s35, 29
	s_add_i32 s34, s34, s35
	s_ashr_i32 s41, s34, 3
	v_cmp_le_i32_e32 vcc, s41, v3
	s_and_saveexec_b64 s[34:35], vcc
	s_xor_b64 s[34:35], exec, s[34:35]
	v_subrev_u32_e32 v3, s41, v3
	s_andn2_saveexec_b64 s[34:35], s[34:35]
	v_lshlrev_b32_e32 v4, 3, v3
	v_add_u32_e32 v2, s37, v4
	v_sub_u32_e32 v4, s36, v4
	v_min_i32_e32 v7, 8, v4
	s_or_b64 exec, exec, s[34:35]
	v_mov_b64_e32 v[66:67], 6
	s_mov_b64 s[36:37], -1
	s_and_saveexec_b64 s[34:35], vcc
	s_cbranch_execz .LBB2_51
	s_lshl_b32 s39, s39, 5
	s_sub_i32 s38, s38, s39
	s_add_i32 s36, s38, 7
	s_ashr_i32 s37, s36, 31
	s_lshr_b32 s37, s37, 29
	s_add_i32 s36, s36, s37
	s_ashr_i32 s41, s36, 3
	v_cmp_le_i32_e32 vcc, s41, v3
	s_and_saveexec_b64 s[36:37], vcc
	s_xor_b64 s[36:37], exec, s[36:37]
	v_subrev_u32_e32 v3, s41, v3
	s_andn2_saveexec_b64 s[36:37], s[36:37]
	v_lshlrev_b32_e32 v4, 3, v3
	v_add_u32_e32 v2, s39, v4
	v_sub_u32_e32 v4, s38, v4
	v_min_i32_e32 v7, 8, v4
	s_or_b64 exec, exec, s[36:37]
	v_mov_b64_e32 v[66:67], 7
	s_mov_b64 s[38:39], -1
	s_and_saveexec_b64 s[36:37], vcc
	s_cbranch_execz .LBB2_50
	s_lshl_b32 s38, s40, 5
	s_sub_i32 s33, s33, s38
	s_add_i32 s39, s33, 7
	s_ashr_i32 s40, s39, 31
	s_lshr_b32 s40, s40, 29
	s_add_i32 s39, s39, s40
	v_lshlrev_b32_e32 v4, 3, v3
	s_ashr_i32 s39, s39, 3
	v_add_u32_e32 v5, s38, v4
	v_sub_u32_e32 v4, s33, v4
	v_min_i32_e32 v4, 8, v4
	v_cmp_gt_i32_e32 vcc, s39, v3
	s_orn2_b64 s[38:39], vcc, exec
	s_nop 0
	v_cndmask_b32_e32 v7, v7, v4, vcc
	v_cndmask_b32_e32 v2, v2, v5, vcc
	v_cndmask_b32_e64 v66, 9, 8, vcc

.LBB2_66:
	s_or_b64 exec, exec, s[2:3]
	s_waitcnt vmcnt(0)
	ds_write_b32 v6, v8 offset:17408
	ds_write_b32 v6, v9 offset:17920
	ds_write_b32 v6, v10 offset:18432
	ds_write_b32 v6, v11 offset:18944
	ds_write_b32 v6, v12 offset:19456
	ds_write_b32 v6, v13 offset:19968
	s_waitcnt lgkmcnt(0)
	s_barrier
	s_and_saveexec_b64 s[2:3], s[4:5]
	s_cbranch_execz .LBB2_134
	v_and_b32_e32 v146, 63, v0
	v_cmp_lt_i32_e32 vcc, v146, v7
	v_mov_b32_e32 v4, -1
	s_and_saveexec_b64 s[2:3], vcc
	s_cbranch_execz .LBB2_69
	s_load_dwordx2 s[4:5], s[0:1], 0x88
	s_mov_b32 s6, 0x61a80
	v_ashrrev_i32_e32 v3, 31, v2
	v_lshlrev_b32_e32 v4, 2, v146
	v_mov_b32_e32 v5, 0
	s_waitcnt lgkmcnt(0)
	v_mov_b64_e32 v[8:9], s[4:5]
	v_mad_u64_u32 v[8:9], s[4:5], v66, s6, v[8:9]
	v_lshl_add_u64 v[2:3], v[2:3], 2, v[8:9]
	v_lshl_add_u64 v[2:3], v[2:3], 0, v[4:5]
	global_load_dword v4, v[2:3], off
